# adds: MFMA skip for all-padding row blocks of expert tiles, 4096-item w_down copy tail in the gate/up phase (2048 items moved to the attention phase)
# baseline (speedup 1.0000x reference)
; #define LAS __attribute__((address_space(3)))
; __global__ void __launch_bounds__(512, 2) hymba_fwd(Args args) {
;     ...
;         LAS unsigned char* vbuf = lds + wave * 12288;
;         {
;             constexpr int CV_LO = CV_N1, CV_HI = CV_GU + CV_D - CV_N5, CV_EXP = CV_HI - CV_LO;
;             const int nA = (512 - bx + G - 1) / G;
;             const int per_wave = (CV_EXP + NGW - 1) / NGW;
;             const int c_lo = CV_LO + gw * per_wave, c_hi = (c_lo + per_wave < CV_HI) ? c_lo + per_wave : CV_HI;
;             const int nsteps = nA > 0 ? nA : 1, per_batch = (per_wave + nsteps - 1) / nsteps;
;             int ia = 0, ic = c_lo;
.LBB0_212:
	s_or_b64 exec, exec, s[0:1]
	s_abs_i32 s0, s3
	v_cvt_f32_u32_e32 v1, s0
	s_mul_i32 s1, s92, 0x3000
	s_add_i32 s68, s1, 0
	s_sub_i32 s1, s3, s2
	v_rcp_iflag_f32_e32 v1, v1
	s_add_i32 s6, s1, 0x1ff
	s_sub_i32 s1, 0xfffffe01, s1
	s_xor_b32 s7, s6, s3
	v_mul_f32_e32 v1, 0x4f7ffffe, v1
	v_cvt_u32_f32_e32 v1, v1
	s_max_i32 s1, s6, s1
	s_sub_i32 s6, 0, s0
	s_ashr_i32 s7, s7, 31
	v_readfirstlane_b32 s20, v1
	s_mul_i32 s6, s6, s20
	s_mul_hi_u32 s6, s20, s6
	s_add_i32 s20, s20, s6
	s_mul_hi_u32 s6, s1, s20
	s_mul_i32 s20, s6, s0
	s_sub_i32 s1, s1, s20
	s_add_i32 s20, s6, 1
	s_sub_i32 s21, s1, s0
	s_cmp_ge_u32 s1, s0
	s_cselect_b32 s6, s20, s6
	s_cselect_b32 s1, s21, s1
	s_add_i32 s20, s6, 1
	s_cmp_ge_u32 s1, s0
	s_cselect_b32 s0, s20, s6
	s_abs_i32 s6, s90
	v_cvt_f32_u32_e32 v1, s6
	s_sub_i32 s20, 0, s6
	s_xor_b32 s0, s0, s7
	s_sub_i32 s69, s0, s7
	v_rcp_iflag_f32_e32 v1, v1
	s_add_i32 s0, s90, 0x37ff
	s_xor_b32 s7, s0, s90
	s_abs_i32 s0, s0
	v_mul_f32_e32 v1, 0x4f7ffffe, v1
	v_cvt_u32_f32_e32 v1, v1
	s_ashr_i32 s7, s7, 31
	v_lshlrev_b32_e32 v4, 1, v159
	v_lshrrev_b32_e32 v3, 2, v159
	v_readfirstlane_b32 s21, v1
	s_mul_i32 s20, s20, s21
	s_mul_hi_u32 s20, s21, s20
	s_add_i32 s21, s21, s20
	s_mul_hi_u32 s20, s0, s21
	s_mul_i32 s21, s20, s6
	s_sub_i32 s0, s0, s21
	s_add_i32 s21, s20, 1
	s_sub_i32 s22, s0, s6
	s_cmp_ge_u32 s0, s6
	s_cselect_b32 s20, s21, s20
	s_cselect_b32 s0, s22, s0
	s_add_i32 s21, s20, 1
	s_cmp_ge_u32 s0, s6
	s_cselect_b32 s0, s21, s20
	s_max_i32 s6, s69, 1
	v_cvt_f32_u32_e32 v1, s6
	s_xor_b32 s0, s0, s7
	s_sub_i32 s0, s0, s7
	s_mul_i32 s7, s0, s34
	v_rcp_iflag_f32_e32 v1, v1
	v_and_b32_e32 v4, 32, v4
	s_add_i32 s67, s7, 0x7800
	s_sub_i32 s20, 0, s6
	v_mul_f32_e32 v1, 0x4f7ffffe, v1
	v_cvt_u32_f32_e32 v1, v1
	s_add_i32 s7, s67, s0
	s_add_i32 s0, s6, s0
	s_add_i32 s0, s0, -1
	v_readfirstlane_b32 s21, v1
	v_lshlrev_b32_e32 v1, 3, v159
	v_and_b32_e32 v2, 0x1c0, v1
	v_add_u32_e32 v163, s68, v2
	v_and_b32_e32 v165, 56, v1
	v_bfe_u32 v2, v0, 2, 2
	v_and_b32_e32 v1, 24, v1
	v_add3_u32 v167, s68, v4, v1
	v_and_or_b32 v1, v3, 8, v2
	s_mul_i32 s20, s20, s21
	v_lshlrev_b32_e32 v169, 6, v1
	v_lshlrev_b32_e32 v1, 8, v159
	s_mul_hi_u32 s20, s21, s20
	v_and_b32_e32 v1, 0x1f00, v1
	v_lshrrev_b32_e32 v2, 5, v159
	s_min_i32 s66, s7, 0xb000
	s_ashr_i32 s7, s0, 31
	s_abs_i32 s0, s0
	s_add_i32 s21, s21, s20
	v_add_u32_e32 v204, s68, v1
	v_and_b32_e32 v1, 15, v0
	v_bitop3_b32 v3, v2, v0, 15 bitop3:0x78
	s_mul_hi_u32 s20, s0, s21
	v_lshlrev_b32_e32 v205, 4, v3
	v_bitop3_b32 v3, v2, v1, 2 bitop3:0x36
	s_mul_i32 s21, s20, s6
	v_lshlrev_b32_e32 v206, 4, v3
	v_bitop3_b32 v3, v2, v1, 4 bitop3:0x36
	s_sub_i32 s0, s0, s21
	v_lshlrev_b32_e32 v207, 4, v3
	v_bitop3_b32 v3, v2, v1, 6 bitop3:0x36
	s_add_i32 s21, s20, 1
	s_sub_i32 s22, s0, s6
	v_lshlrev_b32_e32 v208, 4, v3
	v_bitop3_b32 v3, v2, v1, 8 bitop3:0x36
	s_cmp_ge_u32 s0, s6
	v_lshlrev_b32_e32 v209, 4, v3
	v_bitop3_b32 v3, v2, v1, 10 bitop3:0x36
	s_cselect_b32 s20, s21, s20
	v_lshlrev_b32_e32 v210, 4, v3
	v_bitop3_b32 v3, v2, v1, 12 bitop3:0x36
	v_bitop3_b32 v1, v2, v1, 14 bitop3:0x36
	v_and_b32_e32 v0, 7, v0
	s_cselect_b32 s0, s22, s0
	s_add_i32 s21, s20, 1
	v_lshrrev_b32_e32 v158, 3, v159
	v_lshlrev_b32_e32 v212, 4, v1
	v_lshlrev_b32_e32 v1, 1, v0
	s_cmp_ge_u32 s0, s6
	v_lshlrev_b32_e32 v160, 4, v0
	v_xor_b32_e32 v0, v158, v1
	s_cselect_b32 s0, s21, s20
	v_lshlrev_b32_e32 v214, 4, v0
	v_bitop3_b32 v0, v1, v158, 1 bitop3:0x36
	s_xor_b32 s0, s0, s7
	v_or_b32_e32 v2, 1, v1
	v_lshlrev_b32_e32 v215, 4, v0
	v_bitop3_b32 v0, v158, v1, 8 bitop3:0x36
	s_sub_i32 s72, s0, s7
	s_lshl_b32 s73, s6, 1
	v_lshlrev_b32_e32 v217, 4, v0
	v_bitop3_b32 v0, v158, v2, 8 bitop3:0x36
	v_or_b32_e32 v166, 24, v158
	s_cmpk_gt_u32 s74, 0xff
	v_lshlrev_b32_e32 v218, 4, v0
	v_bitop3_b32 v0, v166, v1, 15 bitop3:0x6c
	v_mov_b32_e32 v171, 0
	v_or_b32_e32 v162, 8, v158
	v_or_b32_e32 v164, 16, v158
	v_lshlrev_b32_e32 v221, 4, v0
	v_bitop3_b32 v0, v166, v2, 15 bitop3:0x6c
	s_cselect_b64 s[6:7], -1, 0
	s_mov_b32 s20, 0x3f803f80
	s_mov_b32 s1, 0
	s_mov_b32 s96, s74
	v_and_b32_e32 v168, 28, v157
	v_lshlrev_b32_e32 v211, 4, v3
	v_mov_b32_e32 v161, v171
	v_lshl_add_u32 v213, v158, 8, s68
	v_lshl_add_u32 v216, v162, 8, s68
	v_lshl_add_u32 v219, v164, 8, s68
	v_lshl_add_u32 v220, v166, 8, s68
	v_lshlrev_b32_e32 v222, 4, v0
	v_cndmask_b32_e64 v223, 0, 1, s[6:7]
	s_movk_i32 s74, 0x60
	s_add_i32 s75, 0, 0x180b4
	s_mov_b32 s76, 0x5fc0000
	s_mov_b32 s77, 0x6fc0000
	s_mov_b32 s78, 0x5fd0000
	s_mov_b32 s79, 0x6fd0000
	s_mov_b32 s80, 0x5fe0000
	s_mov_b32 s81, 0x6fe0000
	s_mov_b32 s40, 0x3f803f80
	s_mov_b32 s41, s20
	s_mov_b32 s42, s20
	s_mov_b32 s43, s20
	v_mov_b32_e32 v0, 0x3f803f80
	s_mov_b32 s82, 0
	s_mov_b32 s83, 0
	s_waitcnt lgkmcnt(0)
	s_barrier
	s_branch .LBB0_214

; __device__ __forceinline__ int lane_id_v() { int l; asm volatile("v_mbcnt_lo_u32_b32 %0, -1, 0\n\tv_mbcnt_hi_u32_b32 %0, -1, %0" : "=v"(l)); return l; }
; __device__ __forceinline__ XItem xitem(const float* w_gate, const float* w_up, const float* w_down, bf16* BTGU, bf16* BTD, int r) {
;     ...
;     { const int per = (DFF / 128) * (DM / 32); const int e = r / per, r3 = r % per; const int nblk = DM / 32, kb = r3 / nblk, nb = r3 % nblk;
;         it.src = w_down + (size_t)e * DFF * DM + (size_t)(128 * kb) * DM + 32 * nb; it.ldw = DM; it.dst = (unsigned char*)BTD + ((size_t)e * DM + 32 * nb) * DFF + 128 * kb; it.ldd = DFF; it.f8 = 1; return it; }
; __global__ void __launch_bounds__(512, 2) hymba_fwd(Args args) {
;     ...
;                 const int units = tb[32] * 8, rem = units % G; int tailb = rem > 0 ? G - rem : G, ti = rem > 0 ? bx - rem : bx;
;                 if (tb[66]) { if (tb[67] > 0) { tailb = tb[67]; ti = tb[68]; } else { tailb = G; ti = bx; } }
;                 if (ti >= 0) { const int lane = lane_id_v(); const int q = (CV_N5 + tailb * 8 - 1) / (tailb * 8), x0 = (ti * 8 + wave) * q, x1 = (x0 + q < CV_N5) ? x0 + q : CV_N5;
;                     convert_range(args.w_gate, args.w_up, args.w_down, BTGU, BTD, CV_GU + CV_D - CV_N5 + x0, CV_GU + CV_D - CV_N5 + x1, lds + wave * 8448, lane); }
.LBB0_757:
	s_lshl_b32 s5, s5, 3
	s_abs_i32 s6, s5
	v_cvt_f32_u32_e32 v0, s6
	s_sub_i32 s8, 0, s6
	s_add_i32 s7, s5, 0xfff
	s_xor_b32 s5, s7, s5
	v_rcp_iflag_f32_e32 v0, v0
	s_abs_i32 s7, s7
	s_ashr_i32 s5, s5, 31
	v_mbcnt_lo_u32_b32 v64, -1, 0
	v_mbcnt_hi_u32_b32 v64, -1, v64
	v_mul_f32_e32 v0, 0x4f7ffffe, v0
	v_cvt_u32_f32_e32 v0, v0
	s_nop 0
	v_readfirstlane_b32 s9, v0
	s_mul_i32 s8, s8, s9
	s_mul_hi_u32 s8, s9, s8
	s_add_i32 s9, s9, s8
	s_mul_hi_u32 s8, s7, s9
	s_mul_i32 s9, s8, s6
	s_sub_i32 s7, s7, s9
	s_add_i32 s10, s8, 1
	s_sub_i32 s9, s7, s6
	s_cmp_ge_u32 s7, s6
	s_cselect_b32 s8, s10, s8
	s_cselect_b32 s7, s9, s7
	s_add_i32 s9, s8, 1
	s_cmp_ge_u32 s7, s6
	s_cselect_b32 s6, s9, s8
	s_lshl_b32 s4, s4, 3
	s_xor_b32 s6, s6, s5
	s_sub_i32 s5, s6, s5
	s_add_i32 s4, s4, s92
	s_mul_i32 s4, s5, s4
	s_add_i32 s5, s4, s5
	s_min_i32 s16, s5, 0x1000
	s_cmp_ge_i32 s4, s16
	s_cbranch_scc1 .LBB0_783
	s_add_i32 s10, s4, 0xb000
	s_cmpk_gt_i32 s4, 0xcfff
	s_cbranch_scc0 .LBB0_762
	s_addk_i32 s4, 0x3000
	s_lshr_b32 s4, s4, 9
	s_mov_b32 s5, 0
	s_lshl_b64 s[6:7], s[4:5], 23
	s_add_u32 s6, s58, s6
	s_addc_u32 s7, s59, s7
	s_lshl_b32 s8, s10, 1
	s_and_b32 s11, s8, 0x380
	s_lshl_b32 s8, s11, 13
	s_add_u32 s6, s6, s8
	s_addc_u32 s7, s7, 0
	s_lshl_b32 s8, s10, 5
	s_and_b32 s12, s8, 0x7e0
	s_lshl_b32 s8, s12, 2
	s_add_u32 s8, s6, s8
	s_addc_u32 s9, s7, 0
	s_lshl_b64 s[4:5], s[4:5], 21
	s_lshl_b32 s6, s12, 10
	s_add_u32 s4, s70, s4
	s_addc_u32 s5, s71, s5
	s_add_u32 s4, s4, s6
	s_addc_u32 s5, s5, 0
	s_add_u32 s6, s4, s11
	s_addc_u32 s7, s5, 0
	s_mov_b64 s[4:5], 0
	s_branch .LBB0_763

; #define LAS __attribute__((address_space(3)))
; __device__ __forceinline__ unsigned cvt_pk_bf16(float lo, float hi) { unsigned r; asm volatile("v_cvt_pk_bf16_f32 %0, %1, %2" : "=v"(r) : "v"(lo), "v"(hi)); return r; }
; __device__ __forceinline__ void t64_load(const float* Wsrc, int ldw, int lane, f32x4 (&tv)[16]) {
;     const float* p = Wsrc + (size_t)(lane >> 3) * ldw + 4 * (lane & 7);
; #pragma unroll
;     for (int i = 0; i < 16; ++i) { tv[i] = __builtin_nontemporal_load((const f32x4*)p); p += 8 * ldw; }
; }
; __device__ __forceinline__ void t64_finish(const f32x4 (&tv)[16], unsigned char* dst, int ldd, int f8, LAS unsigned char* scr, int lane) {
;     const int g = lane >> 4, i16 = lane & 15;
; #pragma unroll
;     for (int i = 0; i < 16; ++i) { v2u w; w.x = cvt_pk_bf16(tv[i].x, tv[i].y); w.y = cvt_pk_bf16(tv[i].z, tv[i].w); *(LAS v2u*)(scr + (8 * i + (lane >> 3)) * 64 + 8 * (lane & 7)) = w; }
; __device__ __forceinline__ void convert_range(const float* w_gate, const float* w_up, const float* w_down, bf16* BTGU, bf16* BTD, int x0, int x1, LAS unsigned char* scr, int lane) {
;     if (x0 >= x1) return;
;     f32x4 ta[16], tc[16];
;     XItem A = xitem(w_gate, w_up, w_down, BTGU, BTD, x0), B = A;
;     t64_load(A.src, A.ldw, lane, ta);
.LBB0_765:
	v_ashrrev_i32_e32 v128, 3, v64
	v_lshlrev_b32_e32 v0, 2, v64
	v_and_b32_e32 v130, 28, v0
	v_mad_i64_i32 v[0:1], s[12:13], s4, v128, 0
	v_mov_b32_e32 v133, 0
	v_lshl_add_u64 v[0:1], v[0:1], 2, s[8:9]
	v_lshlrev_b32_e32 v132, 2, v130
	s_mov_b32 s5, 0
	v_lshl_add_u64 v[40:41], v[0:1], 0, v[132:133]
	s_lshl_b32 s4, s4, 5
	v_lshl_add_u64 v[42:43], v[40:41], 0, s[4:5]
	v_lshl_add_u64 v[66:67], v[42:43], 0, s[4:5]
	v_lshl_add_u64 v[68:69], v[66:67], 0, s[4:5]
	v_lshl_add_u64 v[70:71], v[68:69], 0, s[4:5]
	v_lshl_add_u64 v[72:73], v[70:71], 0, s[4:5]
	v_lshl_add_u64 v[74:75], v[72:73], 0, s[4:5]
	v_lshl_add_u64 v[76:77], v[74:75], 0, s[4:5]
	v_lshl_add_u64 v[78:79], v[76:77], 0, s[4:5]
	v_lshl_add_u64 v[80:81], v[78:79], 0, s[4:5]
	v_lshl_add_u64 v[82:83], v[80:81], 0, s[4:5]
	v_lshl_add_u64 v[84:85], v[82:83], 0, s[4:5]
	v_lshl_add_u64 v[86:87], v[84:85], 0, s[4:5]
	v_lshl_add_u64 v[88:89], v[86:87], 0, s[4:5]
	v_lshl_add_u64 v[90:91], v[88:89], 0, s[4:5]
	v_lshl_add_u64 v[92:93], v[90:91], 0, s[4:5]
	global_load_dwordx4 v[60:63], v[92:93], off nt
	global_load_dwordx4 v[56:59], v[90:91], off nt
	global_load_dwordx4 v[52:55], v[88:89], off nt
	global_load_dwordx4 v[48:51], v[86:87], off nt
	global_load_dwordx4 v[44:47], v[84:85], off nt
	global_load_dwordx4 v[36:39], v[82:83], off nt
	global_load_dwordx4 v[32:35], v[80:81], off nt
	global_load_dwordx4 v[28:31], v[78:79], off nt
	global_load_dwordx4 v[24:27], v[76:77], off nt
	global_load_dwordx4 v[20:23], v[74:75], off nt
	global_load_dwordx4 v[16:19], v[72:73], off nt
	global_load_dwordx4 v[12:15], v[70:71], off nt
	global_load_dwordx4 v[8:11], v[68:69], off nt
	global_load_dwordx4 v[4:7], v[66:67], off nt
	global_load_dwordx4 v[0:3], v[42:43], off nt
	s_nop 0
	global_load_dwordx4 v[40:43], v[40:41], off nt
	v_ashrrev_i32_e32 v68, 4, v64
	v_lshlrev_b32_e32 v70, 2, v68
	v_lshlrev_b32_e32 v71, 5, v68
	v_add_u32_e32 v77, 4, v68
	v_add_u32_e32 v78, 8, v68
	v_add_u32_e32 v79, 12, v68
	v_add_u32_e32 v80, 16, v68
	v_add_u32_e32 v81, 20, v68
	v_add_u32_e32 v82, 24, v68
	v_add_u32_e32 v68, 28, v68
	v_ashrrev_i32_e32 v76, 5, v64
	v_lshrrev_b32_e32 v77, 1, v77
	v_lshrrev_b32_e32 v78, 1, v78
	v_lshrrev_b32_e32 v79, 1, v79
	v_lshrrev_b32_e32 v80, 1, v80
	v_lshrrev_b32_e32 v81, 1, v81
	v_lshrrev_b32_e32 v82, 1, v82
	v_lshrrev_b32_e32 v68, 1, v68
	s_mul_i32 s11, s92, 0x2100
	v_lshlrev_b32_e32 v65, 3, v64
	v_bfe_u32 v69, v64, 2, 2
	v_lshlrev_b32_e32 v75, 8, v64
	v_bitop3_b32 v76, v76, v64, 15 bitop3:0x78
	v_bitop3_b32 v77, v77, v64, 15 bitop3:0x78
	v_bitop3_b32 v78, v78, v64, 15 bitop3:0x78
	v_bitop3_b32 v79, v79, v64, 15 bitop3:0x78
	v_bitop3_b32 v80, v80, v64, 15 bitop3:0x78
	v_bitop3_b32 v81, v81, v64, 15 bitop3:0x78
	v_bitop3_b32 v82, v82, v64, 15 bitop3:0x78
	v_bitop3_b32 v68, v68, v64, 15 bitop3:0x78
	v_and_b32_e32 v64, 7, v64
	s_add_i32 s11, s11, 0
	v_and_b32_e32 v66, 0xffffffc0, v65
	v_and_b32_e32 v67, 56, v65
	v_and_b32_e32 v71, 32, v71
	v_and_b32_e32 v65, 24, v65
	s_mov_b32 s4, 0x3fffff8
	v_lshlrev_b32_e32 v83, 1, v64
	v_add3_u32 v141, s11, v71, v65
	v_and_or_b32 v65, v70, s4, v69
	v_or_b32_e32 v84, 1, v83
	v_lshlrev_b32_e32 v134, 4, v64
	v_and_b32_e32 v64, 15, v128
	v_bitop3_b32 v85, v128, v83, 15 bitop3:0x6c
	v_add_u32_e32 v136, 8, v128
	v_add_u32_e32 v140, 24, v128
	v_lshlrev_b32_e32 v144, 6, v65
	v_and_b32_e32 v75, 0x1f00, v75
	v_lshlrev_b32_e32 v146, 4, v85
	v_bitop3_b32 v64, v83, v64, 1 bitop3:0x36
	v_bitop3_b32 v85, v136, v83, 15 bitop3:0x6c
	v_bitop3_b32 v86, v136, v84, 15 bitop3:0x6c
	v_bitop3_b32 v83, v140, v83, 15 bitop3:0x6c
	v_bitop3_b32 v84, v140, v84, 15 bitop3:0x6c
	s_lshl_b32 s4, s10, 1
	v_add_u32_e32 v66, s11, v66
	v_add_u32_e32 v65, 0x400, v144
	v_add_u32_e32 v69, 0x800, v144
	v_add_u32_e32 v70, 0xc00, v144
	v_add_u32_e32 v71, 0x1000, v144
	v_add_u32_e32 v72, 0x1400, v144
	v_add_u32_e32 v73, 0x1800, v144
	v_add_u32_e32 v74, 0x1c00, v144
	v_add_u32_e32 v75, s11, v75
	v_lshlrev_b32_e32 v76, 4, v76
	v_lshlrev_b32_e32 v77, 4, v77
	v_lshlrev_b32_e32 v78, 4, v78
	v_lshlrev_b32_e32 v79, 4, v79
	v_lshlrev_b32_e32 v80, 4, v80
	v_lshlrev_b32_e32 v81, 4, v81
	v_lshlrev_b32_e32 v82, 4, v82
	v_lshlrev_b32_e32 v68, 4, v68
	v_lshlrev_b32_e32 v147, 4, v64
	v_lshl_add_u32 v64, v136, 8, s11
	v_lshlrev_b32_e32 v85, 4, v85
	v_lshlrev_b32_e32 v86, 4, v86
	v_add_u32_e32 v138, 16, v128
	v_lshl_add_u32 v87, v140, 8, s11
	v_lshlrev_b32_e32 v83, 4, v83
	v_lshlrev_b32_e32 v84, 4, v84
	s_add_i32 s18, s4, 4
	s_lshl_b32 s4, s10, 5
	s_add_i32 s16, s16, 0xb000
	v_ashrrev_i32_e32 v129, 31, v128
	v_mov_b32_e32 v135, v133
	v_lshl_add_u32 v145, v128, 8, s11
	v_ashrrev_i32_e32 v131, 31, v136
	v_lshl_add_u32 v148, v138, 8, s11
	v_ashrrev_i32_e32 v137, 31, v138
	v_ashrrev_i32_e32 v139, 31, v140
	s_add_i32 s20, s10, 0xffff8001
	s_add_i32 s19, s4, 64
	v_add_u32_e32 v149, v66, v67
	v_add_u32_e32 v150, v141, v65
	v_add_u32_e32 v151, v141, v69
	v_add_u32_e32 v152, v141, v70
	v_add_u32_e32 v153, v141, v71
	v_add_u32_e32 v154, v141, v72
	v_add_u32_e32 v155, v141, v73
	v_add_u32_e32 v156, v141, v74
	v_add_u32_e32 v157, v75, v76
	v_add_u32_e32 v158, v75, v77
	v_add_u32_e32 v159, v75, v78
	v_add_u32_e32 v160, v75, v79
	v_add_u32_e32 v161, v75, v80
	v_add_u32_e32 v162, v75, v81
	v_add_u32_e32 v163, v75, v82
	v_add_u32_e32 v164, v75, v68
	v_add_u32_e32 v165, v64, v85
	v_add_u32_e32 v166, v64, v86
	v_add_u32_e32 v167, v87, v83
	v_add_u32_e32 v168, v87, v84
	s_mov_b32 s14, s17
	s_mov_b64 s[8:9], s[6:7]
	s_branch .LBB0_770
